# grid barrier: L1 invalidate issued by the polling wave right after its arrival atomic has returned (leader: after raising the flag), waited once at the end
# speedup vs baseline: 1.0026x; 1.0020x over previous
; __device__ __forceinline__ unsigned xb_ld(unsigned* p)              { return __hip_atomic_load(p, __ATOMIC_RELAXED, __HIP_MEMORY_SCOPE_AGENT); }
; __device__ __forceinline__ unsigned xb_add(unsigned* p, unsigned v) { return __hip_atomic_fetch_add(p, v, __ATOMIC_RELAXED, __HIP_MEMORY_SCOPE_AGENT); }
; #define XB_SPIN(cond, bar) do { unsigned _sp = 0; while (cond) { __builtin_amdgcn_s_sleep(1); \
;     if ((++_sp & 255u) == 0u) { if (xb_ld(&(bar)[XB_TMO])) break; if (_sp > XB_SPIN_CAP) { atomicAdd(&(bar)[XB_TMO], 1u); break; } } } } while (0)
; __device__ __forceinline__ void xcd_barrier(const XcdBarrier& b) {
;     ...
;             else XB_SPIN(xb_ld(&bar[XB_TOPGEN]) == tg, bar);
;             __builtin_amdgcn_fence(__ATOMIC_ACQUIRE, "agent");
;             xb_add(&bar[XB_XGEN(b.x)], 1u);
;             asm volatile("s_waitcnt vmcnt(0)" ::: "memory");
;         } else {
;             XB_SPIN(xb_ld(&bar[XB_XGEN(b.x)]) == gen, bar);
;             __builtin_amdgcn_fence(__ATOMIC_ACQUIRE, "agent");
.Lgb0_poll:
	buffer_inv sc1
	v_readfirstlane_b32 s10, v4
	v_readfirstlane_b32 s11, v3
	s_mov_b64 exec, 0xffff
	v_lshlrev_b32_e32 v5, 2, v0
	s_mov_b32 s12, 0

; __device__ __forceinline__ unsigned xb_ld(unsigned* p)              { return __hip_atomic_load(p, __ATOMIC_RELAXED, __HIP_MEMORY_SCOPE_AGENT); }
; #define XB_SPIN(cond, bar) do { unsigned _sp = 0; while (cond) { __builtin_amdgcn_s_sleep(1); \
;     if ((++_sp & 255u) == 0u) { if (xb_ld(&(bar)[XB_TMO])) break; if (_sp > XB_SPIN_CAP) { atomicAdd(&(bar)[XB_TMO], 1u); break; } } } } while (0)
; __device__ __forceinline__ void xcd_barrier(const XcdBarrier& b) {
;     ...
;             XB_SPIN(xb_ld(&bar[XB_XGEN(b.x)]) == gen, bar);
;             __builtin_amdgcn_fence(__ATOMIC_ACQUIRE, "agent");
;             asm volatile("s_waitcnt vmcnt(0)" ::: "memory");
;         }
;     }
;     __syncthreads();
.Lgb0_done:
	s_waitcnt vmcnt(0) lgkmcnt(0)
.LBB0_142:
	s_or_b64 exec, exec, s[0:1]
	s_waitcnt lgkmcnt(0)
	s_barrier

; __device__ __forceinline__ unsigned xb_ld(unsigned* p)              { return __hip_atomic_load(p, __ATOMIC_RELAXED, __HIP_MEMORY_SCOPE_AGENT); }
; #define XB_SPIN(cond, bar) do { unsigned _sp = 0; while (cond) { __builtin_amdgcn_s_sleep(1); \
;     if ((++_sp & 255u) == 0u) { if (xb_ld(&(bar)[XB_TMO])) break; if (_sp > XB_SPIN_CAP) { atomicAdd(&(bar)[XB_TMO], 1u); break; } } } } while (0)
; __device__ __forceinline__ void xcd_barrier(const XcdBarrier& b) {
;     ...
;             XB_SPIN(xb_ld(&bar[XB_XGEN(b.x)]) == gen, bar);
;             __builtin_amdgcn_fence(__ATOMIC_ACQUIRE, "agent");
;             asm volatile("s_waitcnt vmcnt(0)" ::: "memory");
;         }
;     }
;     __syncthreads();
.Lgb1_done:
	s_waitcnt vmcnt(0) lgkmcnt(0)
.LBB0_763:
	s_or_b64 exec, exec, s[0:1]
	s_waitcnt lgkmcnt(0)
	s_barrier

; __device__ __forceinline__ unsigned xb_ld(unsigned* p)              { return __hip_atomic_load(p, __ATOMIC_RELAXED, __HIP_MEMORY_SCOPE_AGENT); }
; #define XB_SPIN(cond, bar) do { unsigned _sp = 0; while (cond) { __builtin_amdgcn_s_sleep(1); \
;     if ((++_sp & 255u) == 0u) { if (xb_ld(&(bar)[XB_TMO])) break; if (_sp > XB_SPIN_CAP) { atomicAdd(&(bar)[XB_TMO], 1u); break; } } } } while (0)
; __device__ __forceinline__ void xcd_barrier(const XcdBarrier& b) {
;     ...
;             XB_SPIN(xb_ld(&bar[XB_XGEN(b.x)]) == gen, bar);
;             __builtin_amdgcn_fence(__ATOMIC_ACQUIRE, "agent");
;             asm volatile("s_waitcnt vmcnt(0)" ::: "memory");
;         }
;     }
;     __syncthreads();
.Lgb2_done:
	s_waitcnt vmcnt(0) lgkmcnt(0)
.LBB0_920:
	s_or_b64 exec, exec, s[0:1]
	s_waitcnt lgkmcnt(0)
	s_barrier

; __device__ __forceinline__ unsigned xb_ld(unsigned* p)              { return __hip_atomic_load(p, __ATOMIC_RELAXED, __HIP_MEMORY_SCOPE_AGENT); }
; #define XB_SPIN(cond, bar) do { unsigned _sp = 0; while (cond) { __builtin_amdgcn_s_sleep(1); \
;     if ((++_sp & 255u) == 0u) { if (xb_ld(&(bar)[XB_TMO])) break; if (_sp > XB_SPIN_CAP) { atomicAdd(&(bar)[XB_TMO], 1u); break; } } } } while (0)
; __device__ __forceinline__ void xcd_barrier(const XcdBarrier& b) {
;     ...
;             XB_SPIN(xb_ld(&bar[XB_XGEN(b.x)]) == gen, bar);
;             __builtin_amdgcn_fence(__ATOMIC_ACQUIRE, "agent");
;             asm volatile("s_waitcnt vmcnt(0)" ::: "memory");
;         }
;     }
;     __syncthreads();
.Lgb3_done:
	s_waitcnt vmcnt(0) lgkmcnt(0)
.LBB0_1002:
	s_or_b64 exec, exec, s[0:1]
	s_waitcnt lgkmcnt(0)
	s_barrier

; __device__ __forceinline__ unsigned xb_ld(unsigned* p)              { return __hip_atomic_load(p, __ATOMIC_RELAXED, __HIP_MEMORY_SCOPE_AGENT); }
; #define XB_SPIN(cond, bar) do { unsigned _sp = 0; while (cond) { __builtin_amdgcn_s_sleep(1); \
;     if ((++_sp & 255u) == 0u) { if (xb_ld(&(bar)[XB_TMO])) break; if (_sp > XB_SPIN_CAP) { atomicAdd(&(bar)[XB_TMO], 1u); break; } } } } while (0)
; __device__ __forceinline__ void xcd_barrier(const XcdBarrier& b) {
;     ...
;             XB_SPIN(xb_ld(&bar[XB_XGEN(b.x)]) == gen, bar);
;             __builtin_amdgcn_fence(__ATOMIC_ACQUIRE, "agent");
;             asm volatile("s_waitcnt vmcnt(0)" ::: "memory");
;         }
;     }
;     __syncthreads();
.Lgb4_done:
	s_waitcnt vmcnt(0) lgkmcnt(0)
.LBB0_1079:
	s_or_b64 exec, exec, s[0:1]
	s_waitcnt lgkmcnt(0)
	s_barrier

; __device__ __forceinline__ unsigned xb_ld(unsigned* p)              { return __hip_atomic_load(p, __ATOMIC_RELAXED, __HIP_MEMORY_SCOPE_AGENT); }
; #define XB_SPIN(cond, bar) do { unsigned _sp = 0; while (cond) { __builtin_amdgcn_s_sleep(1); \
;     if ((++_sp & 255u) == 0u) { if (xb_ld(&(bar)[XB_TMO])) break; if (_sp > XB_SPIN_CAP) { atomicAdd(&(bar)[XB_TMO], 1u); break; } } } } while (0)
; __device__ __forceinline__ void xcd_barrier(const XcdBarrier& b) {
;     ...
;             XB_SPIN(xb_ld(&bar[XB_XGEN(b.x)]) == gen, bar);
;             __builtin_amdgcn_fence(__ATOMIC_ACQUIRE, "agent");
;             asm volatile("s_waitcnt vmcnt(0)" ::: "memory");
;         }
;     }
;     __syncthreads();
.Lgb5_done:
	s_waitcnt vmcnt(0) lgkmcnt(0)
.LBB0_1151:
	s_or_b64 exec, exec, s[0:1]
	s_waitcnt lgkmcnt(0)
	s_barrier

; __device__ __forceinline__ unsigned xb_ld(unsigned* p)              { return __hip_atomic_load(p, __ATOMIC_RELAXED, __HIP_MEMORY_SCOPE_AGENT); }
; #define XB_SPIN(cond, bar) do { unsigned _sp = 0; while (cond) { __builtin_amdgcn_s_sleep(1); \
;     if ((++_sp & 255u) == 0u) { if (xb_ld(&(bar)[XB_TMO])) break; if (_sp > XB_SPIN_CAP) { atomicAdd(&(bar)[XB_TMO], 1u); break; } } } } while (0)
; __device__ __forceinline__ void xcd_barrier(const XcdBarrier& b) {
;     ...
;             XB_SPIN(xb_ld(&bar[XB_XGEN(b.x)]) == gen, bar);
;             __builtin_amdgcn_fence(__ATOMIC_ACQUIRE, "agent");
;             asm volatile("s_waitcnt vmcnt(0)" ::: "memory");
;         }
;     }
;     __syncthreads();
.Lgb6_done:
	s_waitcnt vmcnt(0) lgkmcnt(0)
.LBB0_1277:
	s_or_b64 exec, exec, s[0:1]
	s_waitcnt lgkmcnt(0)
	s_barrier

; __device__ __forceinline__ unsigned xb_ld(unsigned* p)              { return __hip_atomic_load(p, __ATOMIC_RELAXED, __HIP_MEMORY_SCOPE_AGENT); }
; #define XB_SPIN(cond, bar) do { unsigned _sp = 0; while (cond) { __builtin_amdgcn_s_sleep(1); \
;     if ((++_sp & 255u) == 0u) { if (xb_ld(&(bar)[XB_TMO])) break; if (_sp > XB_SPIN_CAP) { atomicAdd(&(bar)[XB_TMO], 1u); break; } } } } while (0)
; __device__ __forceinline__ void xcd_barrier(const XcdBarrier& b) {
;     ...
;             XB_SPIN(xb_ld(&bar[XB_XGEN(b.x)]) == gen, bar);
;             __builtin_amdgcn_fence(__ATOMIC_ACQUIRE, "agent");
;             asm volatile("s_waitcnt vmcnt(0)" ::: "memory");
;         }
;     }
;     __syncthreads();
.Lgb7_done:
	s_waitcnt vmcnt(0) lgkmcnt(0)
.LBB0_1370:
	s_or_b64 exec, exec, s[0:1]
	s_waitcnt lgkmcnt(0)
	s_barrier

; __device__ __forceinline__ unsigned xb_ld(unsigned* p)              { return __hip_atomic_load(p, __ATOMIC_RELAXED, __HIP_MEMORY_SCOPE_AGENT); }
; #define XB_SPIN(cond, bar) do { unsigned _sp = 0; while (cond) { __builtin_amdgcn_s_sleep(1); \
;     if ((++_sp & 255u) == 0u) { if (xb_ld(&(bar)[XB_TMO])) break; if (_sp > XB_SPIN_CAP) { atomicAdd(&(bar)[XB_TMO], 1u); break; } } } } while (0)
; __device__ __forceinline__ void xcd_barrier(const XcdBarrier& b) {
;     ...
;             XB_SPIN(xb_ld(&bar[XB_XGEN(b.x)]) == gen, bar);
;             __builtin_amdgcn_fence(__ATOMIC_ACQUIRE, "agent");
;             asm volatile("s_waitcnt vmcnt(0)" ::: "memory");
;         }
;     }
;     __syncthreads();
.Lgb8_done:
	s_waitcnt vmcnt(0) lgkmcnt(0)
.LBB0_1461:
	s_or_b64 exec, exec, s[0:1]
	s_waitcnt lgkmcnt(0)
	s_barrier
